# P1 fp8 epilogue rope path: only the 15 vmcnt(0) waits that merely wait for store acknowledgements removed (no prefetch), later code kept at identical byte alignment
# speedup vs baseline: 1.0189x; 1.0189x over previous
.LBB0_381:
	s_add_i32 s30, s30, s49
	v_lshl_add_u32 v18, v18, 3, s30
	v_ashrrev_i32_e32 v19, 31, v18
	v_mul_lo_u32 v30, s75, v16
	v_mul_lo_u32 v17, s74, v17
	v_mad_u64_u32 v[20:21], s[30:31], s74, v16, 0
	v_lshl_add_u64 v[18:19], v[18:19], 1, s[76:77]
	v_add3_u32 v21, v21, v17, v30
	v_lshl_add_u64 v[20:21], v[20:21], 1, v[18:19]
	v_cvt_pk_bf16_f32 v152, v24, v25
	v_cvt_pk_bf16_f32 v153, v22, v23
	v_cvt_pk_bf16_f32 v154, v28, v29
	v_cvt_pk_bf16_f32 v155, v26, v27
	v_pk_mul_f32 v[22:23], v[150:151], s[48:49] op_sel_hi:[1,0]
	v_pk_mul_f32 v[24:25], v[148:149], s[48:49] op_sel_hi:[1,0]
	v_pk_mul_f32 v[26:27], v[146:147], s[48:49] op_sel_hi:[1,0]
	s_and_b64 vcc, exec, s[6:7]
	v_pk_mul_f32 v[28:29], v[144:145], s[48:49] op_sel_hi:[1,0]
	global_store_dwordx4 v[20:21], v[152:155], off
	s_cbranch_vccnz .LBB0_460
	v_and_b32_e32 v30, 64, v186
	v_xor_b32_e32 v17, 32, v186
	v_add_u32_e32 v30, 64, v30
	v_cmp_lt_i32_e32 vcc, v17, v30
	v_mov_b32_e32 v154, v13
	v_mov_b32_e32 v155, v15
	v_cndmask_b32_e32 v17, v186, v17, vcc
	v_lshlrev_b32_e32 v17, 2, v17
	ds_bpermute_b32 v30, v17, v24
	ds_bpermute_b32 v31, v17, v25
	v_mov_b32_e32 v152, v12
	v_mov_b32_e32 v153, v14
	s_waitcnt lgkmcnt(0)
	v_pk_mul_f32 v[30:31], v[154:155], v[30:31]
	s_nop 0
	v_cndmask_b32_e64 v31, v31, -v31, s[4:5]
	v_cndmask_b32_e64 v30, v30, -v30, s[4:5]
	v_pk_fma_f32 v[24:25], v[24:25], v[152:153], v[30:31]
	ds_bpermute_b32 v30, v17, v22
	ds_bpermute_b32 v31, v17, v23
	v_mov_b32_e32 v154, v9
	v_mov_b32_e32 v155, v11
	v_mov_b32_e32 v152, v8
	v_mov_b32_e32 v153, v10
	s_waitcnt lgkmcnt(0)
	v_pk_mul_f32 v[30:31], v[154:155], v[30:31]
	v_mov_b32_e32 v154, v5
	v_cndmask_b32_e64 v31, v31, -v31, s[4:5]
	v_cndmask_b32_e64 v30, v30, -v30, s[4:5]
	v_pk_fma_f32 v[22:23], v[22:23], v[152:153], v[30:31]
	ds_bpermute_b32 v30, v17, v28
	ds_bpermute_b32 v31, v17, v29
	v_mov_b32_e32 v155, v7
	v_mov_b32_e32 v152, v4
	v_mov_b32_e32 v153, v6
	s_waitcnt lgkmcnt(0)
	v_pk_mul_f32 v[30:31], v[154:155], v[30:31]
	s_nop 0
	v_cndmask_b32_e64 v31, v31, -v31, s[4:5]
	v_cndmask_b32_e64 v30, v30, -v30, s[4:5]
	v_pk_fma_f32 v[28:29], v[28:29], v[152:153], v[30:31]
	ds_bpermute_b32 v30, v17, v26
	ds_bpermute_b32 v31, v17, v27
	v_mov_b32_e32 v154, v1
	v_mov_b32_e32 v155, v3
	v_mov_b32_e32 v152, v0
	v_mov_b32_e32 v153, v2
	s_waitcnt lgkmcnt(0)
	v_pk_mul_f32 v[30:31], v[154:155], v[30:31]
	s_nop 0
	v_cndmask_b32_e64 v31, v31, -v31, s[4:5]
	v_cndmask_b32_e64 v30, v30, -v30, s[4:5]
	v_pk_fma_f32 v[26:27], v[26:27], v[152:153], v[30:31]
	s_and_b64 vcc, exec, s[8:9]
	s_cbranch_vccz .LBB0_461

.LBB0_385:
	v_cvt_pk_bf16_f32 v144, v24, v25
	v_cvt_pk_bf16_f32 v145, v22, v23
	v_cvt_pk_bf16_f32 v146, v28, v29
	v_cvt_pk_bf16_f32 v147, v26, v27
	global_store_dwordx4 v[20:21], v[144:147], off offset:256
	v_or_b32_e32 v20, 16, v16
	s_and_b64 vcc, exec, s[6:7]
	v_ashrrev_i32_e32 v21, 31, v20
	s_cbranch_vccnz .LBB0_387
	v_lshlrev_b64 v[0:1], 7, v[20:21]
	v_lshl_add_u64 v[0:1], s[28:29], 0, v[0:1]
	v_lshl_add_u64 v[12:13], v[0:1], 0, v[168:169]
	global_load_dwordx4 v[0:3], v[12:13], off offset:48
	global_load_dwordx4 v[4:7], v[12:13], off offset:32
	global_load_dwordx4 v[8:11], v[12:13], off offset:16
	s_nop 0
	global_load_dwordx4 v[12:15], v[12:13], off

.LBB0_391:
	v_mul_lo_u32 v17, s75, v20
	v_mul_lo_u32 v30, s74, v21
	v_mad_u64_u32 v[20:21], s[30:31], s74, v20, 0
	v_add3_u32 v21, v21, v30, v17
	v_lshl_add_u64 v[20:21], v[20:21], 1, v[18:19]
	v_cvt_pk_bf16_f32 v136, v24, v25
	v_cvt_pk_bf16_f32 v137, v22, v23
	v_cvt_pk_bf16_f32 v138, v28, v29
	v_cvt_pk_bf16_f32 v139, v26, v27
	v_pk_mul_f32 v[22:23], v[134:135], s[48:49] op_sel_hi:[1,0]
	v_pk_mul_f32 v[24:25], v[132:133], s[48:49] op_sel_hi:[1,0]
	v_pk_mul_f32 v[26:27], v[130:131], s[48:49] op_sel_hi:[1,0]
	s_and_b64 vcc, exec, s[6:7]
	v_pk_mul_f32 v[28:29], v[128:129], s[48:49] op_sel_hi:[1,0]
	global_store_dwordx4 v[20:21], v[136:139], off
	s_cbranch_vccnz .LBB0_464
	v_and_b32_e32 v30, 64, v186
	v_xor_b32_e32 v17, 32, v186
	v_add_u32_e32 v30, 64, v30
	v_cmp_lt_i32_e32 vcc, v17, v30
	v_mov_b32_e32 v138, v13
	v_mov_b32_e32 v139, v15
	v_cndmask_b32_e32 v17, v186, v17, vcc
	v_lshlrev_b32_e32 v17, 2, v17
	ds_bpermute_b32 v30, v17, v24
	ds_bpermute_b32 v31, v17, v25
	v_mov_b32_e32 v136, v12
	v_mov_b32_e32 v137, v14
	s_waitcnt lgkmcnt(0)
	v_pk_mul_f32 v[30:31], v[138:139], v[30:31]
	s_nop 0
	v_cndmask_b32_e64 v31, v31, -v31, s[4:5]
	v_cndmask_b32_e64 v30, v30, -v30, s[4:5]
	v_pk_fma_f32 v[24:25], v[24:25], v[136:137], v[30:31]
	ds_bpermute_b32 v30, v17, v22
	ds_bpermute_b32 v31, v17, v23
	v_mov_b32_e32 v138, v9
	v_mov_b32_e32 v139, v11
	v_mov_b32_e32 v136, v8
	v_mov_b32_e32 v137, v10
	s_waitcnt lgkmcnt(0)
	v_pk_mul_f32 v[30:31], v[138:139], v[30:31]
	v_mov_b32_e32 v138, v5
	v_cndmask_b32_e64 v31, v31, -v31, s[4:5]
	v_cndmask_b32_e64 v30, v30, -v30, s[4:5]
	v_pk_fma_f32 v[22:23], v[22:23], v[136:137], v[30:31]
	ds_bpermute_b32 v30, v17, v28
	ds_bpermute_b32 v31, v17, v29
	v_mov_b32_e32 v139, v7
	v_mov_b32_e32 v136, v4
	v_mov_b32_e32 v137, v6
	s_waitcnt lgkmcnt(0)
	v_pk_mul_f32 v[30:31], v[138:139], v[30:31]
	s_nop 0
	v_cndmask_b32_e64 v31, v31, -v31, s[4:5]
	v_cndmask_b32_e64 v30, v30, -v30, s[4:5]
	v_pk_fma_f32 v[28:29], v[28:29], v[136:137], v[30:31]
	ds_bpermute_b32 v30, v17, v26
	ds_bpermute_b32 v31, v17, v27
	v_mov_b32_e32 v138, v1
	v_mov_b32_e32 v139, v3
	v_mov_b32_e32 v136, v0
	v_mov_b32_e32 v137, v2
	s_waitcnt lgkmcnt(0)
	v_pk_mul_f32 v[30:31], v[138:139], v[30:31]
	s_nop 0
	v_cndmask_b32_e64 v31, v31, -v31, s[4:5]
	v_cndmask_b32_e64 v30, v30, -v30, s[4:5]
	v_pk_fma_f32 v[26:27], v[26:27], v[136:137], v[30:31]
	s_and_b64 vcc, exec, s[8:9]
	s_cbranch_vccz .LBB0_465

.LBB0_395:
	v_cvt_pk_bf16_f32 v128, v24, v25
	v_cvt_pk_bf16_f32 v129, v22, v23
	v_cvt_pk_bf16_f32 v130, v28, v29
	v_cvt_pk_bf16_f32 v131, v26, v27
	global_store_dwordx4 v[20:21], v[128:131], off offset:256
	v_or_b32_e32 v20, 32, v16
	s_and_b64 vcc, exec, s[6:7]
	v_ashrrev_i32_e32 v21, 31, v20
	s_cbranch_vccnz .LBB0_397
	v_lshlrev_b64 v[0:1], 7, v[20:21]
	v_lshl_add_u64 v[0:1], s[28:29], 0, v[0:1]
	v_lshl_add_u64 v[12:13], v[0:1], 0, v[168:169]
	global_load_dwordx4 v[0:3], v[12:13], off offset:48
	global_load_dwordx4 v[4:7], v[12:13], off offset:32
	global_load_dwordx4 v[8:11], v[12:13], off offset:16
	s_nop 0
	global_load_dwordx4 v[12:15], v[12:13], off

.LBB0_401:
	v_mul_lo_u32 v17, s75, v20
	v_mul_lo_u32 v30, s74, v21
	v_mad_u64_u32 v[20:21], s[30:31], s74, v20, 0
	v_add3_u32 v21, v21, v30, v17
	v_lshl_add_u64 v[20:21], v[20:21], 1, v[18:19]
	v_cvt_pk_bf16_f32 v120, v24, v25
	v_cvt_pk_bf16_f32 v121, v22, v23
	v_cvt_pk_bf16_f32 v122, v28, v29
	v_cvt_pk_bf16_f32 v123, v26, v27
	v_pk_mul_f32 v[22:23], v[118:119], s[48:49] op_sel_hi:[1,0]
	v_pk_mul_f32 v[24:25], v[116:117], s[48:49] op_sel_hi:[1,0]
	v_pk_mul_f32 v[26:27], v[114:115], s[48:49] op_sel_hi:[1,0]
	s_and_b64 vcc, exec, s[6:7]
	v_pk_mul_f32 v[28:29], v[112:113], s[48:49] op_sel_hi:[1,0]
	global_store_dwordx4 v[20:21], v[120:123], off
	s_cbranch_vccnz .LBB0_468
	v_and_b32_e32 v30, 64, v186
	v_xor_b32_e32 v17, 32, v186
	v_add_u32_e32 v30, 64, v30
	v_cmp_lt_i32_e32 vcc, v17, v30
	v_mov_b32_e32 v122, v13
	v_mov_b32_e32 v123, v15
	v_cndmask_b32_e32 v17, v186, v17, vcc
	v_lshlrev_b32_e32 v17, 2, v17
	ds_bpermute_b32 v30, v17, v24
	ds_bpermute_b32 v31, v17, v25
	v_mov_b32_e32 v120, v12
	v_mov_b32_e32 v121, v14
	s_waitcnt lgkmcnt(0)
	v_pk_mul_f32 v[30:31], v[122:123], v[30:31]
	s_nop 0
	v_cndmask_b32_e64 v31, v31, -v31, s[4:5]
	v_cndmask_b32_e64 v30, v30, -v30, s[4:5]
	v_pk_fma_f32 v[24:25], v[24:25], v[120:121], v[30:31]
	ds_bpermute_b32 v30, v17, v22
	ds_bpermute_b32 v31, v17, v23
	v_mov_b32_e32 v122, v9
	v_mov_b32_e32 v123, v11
	v_mov_b32_e32 v120, v8
	v_mov_b32_e32 v121, v10
	s_waitcnt lgkmcnt(0)
	v_pk_mul_f32 v[30:31], v[122:123], v[30:31]
	v_mov_b32_e32 v122, v5
	v_cndmask_b32_e64 v31, v31, -v31, s[4:5]
	v_cndmask_b32_e64 v30, v30, -v30, s[4:5]
	v_pk_fma_f32 v[22:23], v[22:23], v[120:121], v[30:31]
	ds_bpermute_b32 v30, v17, v28
	ds_bpermute_b32 v31, v17, v29
	v_mov_b32_e32 v123, v7
	v_mov_b32_e32 v120, v4
	v_mov_b32_e32 v121, v6
	s_waitcnt lgkmcnt(0)
	v_pk_mul_f32 v[30:31], v[122:123], v[30:31]
	s_nop 0
	v_cndmask_b32_e64 v31, v31, -v31, s[4:5]
	v_cndmask_b32_e64 v30, v30, -v30, s[4:5]
	v_pk_fma_f32 v[28:29], v[28:29], v[120:121], v[30:31]
	ds_bpermute_b32 v30, v17, v26
	ds_bpermute_b32 v31, v17, v27
	v_mov_b32_e32 v122, v1
	v_mov_b32_e32 v123, v3
	v_mov_b32_e32 v120, v0
	v_mov_b32_e32 v121, v2
	s_waitcnt lgkmcnt(0)
	v_pk_mul_f32 v[30:31], v[122:123], v[30:31]
	s_nop 0
	v_cndmask_b32_e64 v31, v31, -v31, s[4:5]
	v_cndmask_b32_e64 v30, v30, -v30, s[4:5]
	v_pk_fma_f32 v[26:27], v[26:27], v[120:121], v[30:31]
	s_and_b64 vcc, exec, s[8:9]
	s_cbranch_vccz .LBB0_469

.LBB0_405:
	v_cvt_pk_bf16_f32 v112, v24, v25
	v_cvt_pk_bf16_f32 v113, v22, v23
	v_cvt_pk_bf16_f32 v114, v28, v29
	v_cvt_pk_bf16_f32 v115, v26, v27
	global_store_dwordx4 v[20:21], v[112:115], off offset:256
	v_or_b32_e32 v20, 48, v16
	s_and_b64 vcc, exec, s[6:7]
	v_ashrrev_i32_e32 v21, 31, v20
	s_cbranch_vccnz .LBB0_407
	v_lshlrev_b64 v[0:1], 7, v[20:21]
	v_lshl_add_u64 v[0:1], s[28:29], 0, v[0:1]
	v_lshl_add_u64 v[12:13], v[0:1], 0, v[168:169]
	global_load_dwordx4 v[0:3], v[12:13], off offset:48
	global_load_dwordx4 v[4:7], v[12:13], off offset:32
	global_load_dwordx4 v[8:11], v[12:13], off offset:16
	s_nop 0
	global_load_dwordx4 v[12:15], v[12:13], off

.LBB0_415:
	v_cvt_pk_bf16_f32 v96, v24, v25
	v_cvt_pk_bf16_f32 v97, v22, v23
	v_cvt_pk_bf16_f32 v98, v28, v29
	v_cvt_pk_bf16_f32 v99, v26, v27
	global_store_dwordx4 v[20:21], v[96:99], off offset:256
	v_add_u32_e32 v20, 0x80, v16
	s_and_b64 vcc, exec, s[6:7]
	v_ashrrev_i32_e32 v21, 31, v20
	s_cbranch_vccnz .LBB0_417
	v_lshlrev_b64 v[0:1], 7, v[20:21]
	v_lshl_add_u64 v[0:1], s[28:29], 0, v[0:1]
	v_lshl_add_u64 v[12:13], v[0:1], 0, v[168:169]
	global_load_dwordx4 v[0:3], v[12:13], off offset:48
	global_load_dwordx4 v[4:7], v[12:13], off offset:32
	global_load_dwordx4 v[8:11], v[12:13], off offset:16
	s_nop 0
	global_load_dwordx4 v[12:15], v[12:13], off

.LBB0_421:
	v_mul_lo_u32 v17, s75, v20
	v_mul_lo_u32 v30, s74, v21
	v_mad_u64_u32 v[20:21], s[30:31], s74, v20, 0
	v_add3_u32 v21, v21, v30, v17
	v_lshl_add_u64 v[20:21], v[20:21], 1, v[18:19]
	v_cvt_pk_bf16_f32 v88, v24, v25
	v_cvt_pk_bf16_f32 v89, v22, v23
	v_cvt_pk_bf16_f32 v90, v28, v29
	v_cvt_pk_bf16_f32 v91, v26, v27
	v_pk_mul_f32 v[22:23], v[86:87], s[48:49] op_sel_hi:[1,0]
	v_pk_mul_f32 v[24:25], v[84:85], s[48:49] op_sel_hi:[1,0]
	v_pk_mul_f32 v[26:27], v[82:83], s[48:49] op_sel_hi:[1,0]
	s_and_b64 vcc, exec, s[6:7]
	v_pk_mul_f32 v[28:29], v[80:81], s[48:49] op_sel_hi:[1,0]
	global_store_dwordx4 v[20:21], v[88:91], off
	s_cbranch_vccnz .LBB0_476
	v_and_b32_e32 v30, 64, v186
	v_xor_b32_e32 v17, 32, v186
	v_add_u32_e32 v30, 64, v30
	v_cmp_lt_i32_e32 vcc, v17, v30
	v_mov_b32_e32 v90, v13
	v_mov_b32_e32 v91, v15
	v_cndmask_b32_e32 v17, v186, v17, vcc
	v_lshlrev_b32_e32 v17, 2, v17
	ds_bpermute_b32 v30, v17, v24
	ds_bpermute_b32 v31, v17, v25
	v_mov_b32_e32 v88, v12
	v_mov_b32_e32 v89, v14
	s_waitcnt lgkmcnt(0)
	v_pk_mul_f32 v[30:31], v[90:91], v[30:31]
	s_nop 0
	v_cndmask_b32_e64 v31, v31, -v31, s[4:5]
	v_cndmask_b32_e64 v30, v30, -v30, s[4:5]
	v_pk_fma_f32 v[24:25], v[24:25], v[88:89], v[30:31]
	ds_bpermute_b32 v30, v17, v22
	ds_bpermute_b32 v31, v17, v23
	v_mov_b32_e32 v90, v9
	v_mov_b32_e32 v91, v11
	v_mov_b32_e32 v88, v8
	v_mov_b32_e32 v89, v10
	s_waitcnt lgkmcnt(0)
	v_pk_mul_f32 v[30:31], v[90:91], v[30:31]
	v_mov_b32_e32 v90, v5
	v_cndmask_b32_e64 v31, v31, -v31, s[4:5]
	v_cndmask_b32_e64 v30, v30, -v30, s[4:5]
	v_pk_fma_f32 v[22:23], v[22:23], v[88:89], v[30:31]
	ds_bpermute_b32 v30, v17, v28
	ds_bpermute_b32 v31, v17, v29
	v_mov_b32_e32 v91, v7
	v_mov_b32_e32 v88, v4
	v_mov_b32_e32 v89, v6
	s_waitcnt lgkmcnt(0)
	v_pk_mul_f32 v[30:31], v[90:91], v[30:31]
	s_nop 0
	v_cndmask_b32_e64 v31, v31, -v31, s[4:5]
	v_cndmask_b32_e64 v30, v30, -v30, s[4:5]
	v_pk_fma_f32 v[28:29], v[28:29], v[88:89], v[30:31]
	ds_bpermute_b32 v30, v17, v26
	ds_bpermute_b32 v31, v17, v27
	v_mov_b32_e32 v90, v1
	v_mov_b32_e32 v91, v3
	v_mov_b32_e32 v88, v0
	v_mov_b32_e32 v89, v2
	s_waitcnt lgkmcnt(0)
	v_pk_mul_f32 v[30:31], v[90:91], v[30:31]
	s_nop 0
	v_cndmask_b32_e64 v31, v31, -v31, s[4:5]
	v_cndmask_b32_e64 v30, v30, -v30, s[4:5]
	v_pk_fma_f32 v[26:27], v[26:27], v[88:89], v[30:31]
	s_and_b64 vcc, exec, s[8:9]
	s_cbranch_vccz .LBB0_477

.LBB0_425:
	v_cvt_pk_bf16_f32 v80, v24, v25
	v_cvt_pk_bf16_f32 v81, v22, v23
	v_cvt_pk_bf16_f32 v82, v28, v29
	v_cvt_pk_bf16_f32 v83, v26, v27
	global_store_dwordx4 v[20:21], v[80:83], off offset:256
	v_add_u32_e32 v20, 0x90, v16
	s_and_b64 vcc, exec, s[6:7]
	v_ashrrev_i32_e32 v21, 31, v20
	s_cbranch_vccnz .LBB0_427
	v_lshlrev_b64 v[0:1], 7, v[20:21]
	v_lshl_add_u64 v[0:1], s[28:29], 0, v[0:1]
	v_lshl_add_u64 v[12:13], v[0:1], 0, v[168:169]
	global_load_dwordx4 v[0:3], v[12:13], off offset:48
	global_load_dwordx4 v[4:7], v[12:13], off offset:32
	global_load_dwordx4 v[8:11], v[12:13], off offset:16
	s_nop 0
	global_load_dwordx4 v[12:15], v[12:13], off

.LBB0_431:
	v_mul_lo_u32 v17, s75, v20
	v_mul_lo_u32 v30, s74, v21
	v_mad_u64_u32 v[20:21], s[30:31], s74, v20, 0
	v_add3_u32 v21, v21, v30, v17
	v_lshl_add_u64 v[20:21], v[20:21], 1, v[18:19]
	v_cvt_pk_bf16_f32 v72, v24, v25
	v_cvt_pk_bf16_f32 v73, v22, v23
	v_cvt_pk_bf16_f32 v74, v28, v29
	v_cvt_pk_bf16_f32 v75, v26, v27
	v_pk_mul_f32 v[22:23], v[70:71], s[48:49] op_sel_hi:[1,0]
	v_pk_mul_f32 v[24:25], v[68:69], s[48:49] op_sel_hi:[1,0]
	v_pk_mul_f32 v[26:27], v[66:67], s[48:49] op_sel_hi:[1,0]
	s_and_b64 vcc, exec, s[6:7]
	v_pk_mul_f32 v[28:29], v[64:65], s[48:49] op_sel_hi:[1,0]
	global_store_dwordx4 v[20:21], v[72:75], off
	s_cbranch_vccnz .LBB0_480
	v_and_b32_e32 v30, 64, v186
	v_xor_b32_e32 v17, 32, v186
	v_add_u32_e32 v30, 64, v30
	v_cmp_lt_i32_e32 vcc, v17, v30
	v_mov_b32_e32 v74, v13
	v_mov_b32_e32 v75, v15
	v_cndmask_b32_e32 v17, v186, v17, vcc
	v_lshlrev_b32_e32 v17, 2, v17
	ds_bpermute_b32 v30, v17, v24
	ds_bpermute_b32 v31, v17, v25
	v_mov_b32_e32 v72, v12
	v_mov_b32_e32 v73, v14
	s_waitcnt lgkmcnt(0)
	v_pk_mul_f32 v[30:31], v[74:75], v[30:31]
	s_nop 0
	v_cndmask_b32_e64 v31, v31, -v31, s[4:5]
	v_cndmask_b32_e64 v30, v30, -v30, s[4:5]
	v_pk_fma_f32 v[24:25], v[24:25], v[72:73], v[30:31]
	ds_bpermute_b32 v30, v17, v22
	ds_bpermute_b32 v31, v17, v23
	v_mov_b32_e32 v74, v9
	v_mov_b32_e32 v75, v11
	v_mov_b32_e32 v72, v8
	v_mov_b32_e32 v73, v10
	s_waitcnt lgkmcnt(0)
	v_pk_mul_f32 v[30:31], v[74:75], v[30:31]
	v_mov_b32_e32 v74, v5
	v_cndmask_b32_e64 v31, v31, -v31, s[4:5]
	v_cndmask_b32_e64 v30, v30, -v30, s[4:5]
	v_pk_fma_f32 v[22:23], v[22:23], v[72:73], v[30:31]
	ds_bpermute_b32 v30, v17, v28
	ds_bpermute_b32 v31, v17, v29
	v_mov_b32_e32 v75, v7
	v_mov_b32_e32 v72, v4
	v_mov_b32_e32 v73, v6
	s_waitcnt lgkmcnt(0)
	v_pk_mul_f32 v[30:31], v[74:75], v[30:31]
	s_nop 0
	v_cndmask_b32_e64 v31, v31, -v31, s[4:5]
	v_cndmask_b32_e64 v30, v30, -v30, s[4:5]
	v_pk_fma_f32 v[28:29], v[28:29], v[72:73], v[30:31]
	ds_bpermute_b32 v30, v17, v26
	ds_bpermute_b32 v31, v17, v27
	v_mov_b32_e32 v74, v1
	v_mov_b32_e32 v75, v3
	v_mov_b32_e32 v72, v0
	v_mov_b32_e32 v73, v2
	s_waitcnt lgkmcnt(0)
	v_pk_mul_f32 v[30:31], v[74:75], v[30:31]
	s_nop 0
	v_cndmask_b32_e64 v31, v31, -v31, s[4:5]
	v_cndmask_b32_e64 v30, v30, -v30, s[4:5]
	v_pk_fma_f32 v[26:27], v[26:27], v[72:73], v[30:31]
	s_and_b64 vcc, exec, s[8:9]
	s_cbranch_vccz .LBB0_481

.LBB0_435:
	v_cvt_pk_bf16_f32 v64, v24, v25
	v_cvt_pk_bf16_f32 v65, v22, v23
	v_cvt_pk_bf16_f32 v66, v28, v29
	v_cvt_pk_bf16_f32 v67, v26, v27
	global_store_dwordx4 v[20:21], v[64:67], off offset:256
	v_add_u32_e32 v20, 0xa0, v16
	s_and_b64 vcc, exec, s[6:7]
	v_ashrrev_i32_e32 v21, 31, v20
	s_cbranch_vccnz .LBB0_437
	v_lshlrev_b64 v[0:1], 7, v[20:21]
	v_lshl_add_u64 v[0:1], s[28:29], 0, v[0:1]
	v_lshl_add_u64 v[12:13], v[0:1], 0, v[168:169]
	global_load_dwordx4 v[0:3], v[12:13], off offset:48
	global_load_dwordx4 v[4:7], v[12:13], off offset:32
	global_load_dwordx4 v[8:11], v[12:13], off offset:16
	s_nop 0
	global_load_dwordx4 v[12:15], v[12:13], off

.LBB0_441:
	v_mul_lo_u32 v17, s75, v20
	v_mul_lo_u32 v30, s74, v21
	v_mad_u64_u32 v[20:21], s[30:31], s74, v20, 0
	v_add3_u32 v21, v21, v30, v17
	v_lshl_add_u64 v[20:21], v[20:21], 1, v[18:19]
	v_cvt_pk_bf16_f32 v56, v24, v25
	v_cvt_pk_bf16_f32 v57, v22, v23
	v_cvt_pk_bf16_f32 v58, v28, v29
	v_cvt_pk_bf16_f32 v59, v26, v27
	v_pk_mul_f32 v[22:23], v[54:55], s[48:49] op_sel_hi:[1,0]
	v_pk_mul_f32 v[24:25], v[52:53], s[48:49] op_sel_hi:[1,0]
	v_pk_mul_f32 v[26:27], v[50:51], s[48:49] op_sel_hi:[1,0]
	s_and_b64 vcc, exec, s[6:7]
	v_pk_mul_f32 v[28:29], v[48:49], s[48:49] op_sel_hi:[1,0]
	global_store_dwordx4 v[20:21], v[56:59], off
	s_cbranch_vccnz .LBB0_484
	v_and_b32_e32 v30, 64, v186
	v_xor_b32_e32 v17, 32, v186
	v_add_u32_e32 v30, 64, v30
	v_cmp_lt_i32_e32 vcc, v17, v30
	v_mov_b32_e32 v58, v13
	v_mov_b32_e32 v59, v15
	v_cndmask_b32_e32 v17, v186, v17, vcc
	v_lshlrev_b32_e32 v17, 2, v17
	ds_bpermute_b32 v30, v17, v24
	ds_bpermute_b32 v31, v17, v25
	v_mov_b32_e32 v56, v12
	v_mov_b32_e32 v57, v14
	s_waitcnt lgkmcnt(0)
	v_pk_mul_f32 v[30:31], v[58:59], v[30:31]
	s_nop 0
	v_cndmask_b32_e64 v31, v31, -v31, s[4:5]
	v_cndmask_b32_e64 v30, v30, -v30, s[4:5]
	v_pk_fma_f32 v[24:25], v[24:25], v[56:57], v[30:31]
	ds_bpermute_b32 v30, v17, v22
	ds_bpermute_b32 v31, v17, v23
	v_mov_b32_e32 v58, v9
	v_mov_b32_e32 v59, v11
	v_mov_b32_e32 v56, v8
	v_mov_b32_e32 v57, v10
	s_waitcnt lgkmcnt(0)
	v_pk_mul_f32 v[30:31], v[58:59], v[30:31]
	v_mov_b32_e32 v58, v5
	v_cndmask_b32_e64 v31, v31, -v31, s[4:5]
	v_cndmask_b32_e64 v30, v30, -v30, s[4:5]
	v_pk_fma_f32 v[22:23], v[22:23], v[56:57], v[30:31]
	ds_bpermute_b32 v30, v17, v28
	ds_bpermute_b32 v31, v17, v29
	v_mov_b32_e32 v59, v7
	v_mov_b32_e32 v56, v4
	v_mov_b32_e32 v57, v6
	s_waitcnt lgkmcnt(0)
	v_pk_mul_f32 v[30:31], v[58:59], v[30:31]
	s_nop 0
	v_cndmask_b32_e64 v31, v31, -v31, s[4:5]
	v_cndmask_b32_e64 v30, v30, -v30, s[4:5]
	v_pk_fma_f32 v[28:29], v[28:29], v[56:57], v[30:31]
	ds_bpermute_b32 v30, v17, v26
	ds_bpermute_b32 v31, v17, v27
	v_mov_b32_e32 v58, v1
	v_mov_b32_e32 v59, v3
	v_mov_b32_e32 v56, v0
	v_mov_b32_e32 v57, v2
	s_waitcnt lgkmcnt(0)
	v_pk_mul_f32 v[30:31], v[58:59], v[30:31]
	s_nop 0
	v_cndmask_b32_e64 v31, v31, -v31, s[4:5]
	v_cndmask_b32_e64 v30, v30, -v30, s[4:5]
	v_pk_fma_f32 v[26:27], v[26:27], v[56:57], v[30:31]
	s_and_b64 vcc, exec, s[8:9]
	s_cbranch_vccz .LBB0_485

.LBB0_445:
	v_add_u32_e32 v16, 0xb0, v16
	s_and_b64 vcc, exec, s[6:7]
	v_ashrrev_i32_e32 v17, 31, v16
	v_cvt_pk_bf16_f32 v48, v24, v25
	v_cvt_pk_bf16_f32 v49, v22, v23
	v_cvt_pk_bf16_f32 v50, v28, v29
	v_cvt_pk_bf16_f32 v51, v26, v27
	global_store_dwordx4 v[20:21], v[48:51], off offset:256
	s_cbranch_vccnz .LBB0_447
	v_lshlrev_b64 v[0:1], 7, v[16:17]
	v_lshl_add_u64 v[0:1], s[28:29], 0, v[0:1]
	v_lshl_add_u64 v[12:13], v[0:1], 0, v[168:169]
	global_load_dwordx4 v[0:3], v[12:13], off offset:48
	global_load_dwordx4 v[4:7], v[12:13], off offset:32
	global_load_dwordx4 v[8:11], v[12:13], off offset:16
	s_nop 0
	global_load_dwordx4 v[12:15], v[12:13], off

.LBB0_491:
	s_nop 0
	s_nop 0
	s_nop 0
	s_nop 0
	s_nop 0
	s_nop 0
	s_nop 0
	s_nop 0
	s_nop 0
	s_nop 0
	s_nop 0
	s_nop 0
	s_nop 0
	s_nop 0
	s_nop 0
	v_readlane_b32 s4, v251, 10
	v_readlane_b32 s6, v251, 12
	v_readlane_b32 s7, v251, 13
	s_add_u32 s30, s6, 0x100000
	s_addc_u32 s31, s7, 0
	v_readlane_b32 s5, v251, 11
	s_add_u32 s36, s6, 0x4100000
	v_readlane_b32 s0, v251, 0
	s_addc_u32 s37, s7, 0
	s_not_b32 s0, s0
	v_readlane_b32 s4, v251, 19
	s_add_i32 s47, s4, s0
	v_readlane_b32 s1, v251, 1
	s_cmpk_lt_i32 s47, 0x200
	s_cselect_b64 s[0:1], -1, 0
	s_cmpk_gt_i32 s47, 0x1ff
	v_readlane_b32 s5, v251, 20
	v_mbcnt_lo_u32_b32 v8, -1, 0
	v_mbcnt_hi_u32_b32 v8, -1, v8
	s_cbranch_scc1 .LBB0_494
	s_ashr_i32 s4, s47, 31
	s_lshr_b32 s4, s4, 29
	s_add_i32 s8, s47, s4
	s_and_b32 s4, s8, -8
	s_sub_i32 s6, s47, s4
	s_cmp_gt_i32 s6, -1
	s_cbranch_scc0 .LBB0_495
	s_lshl_b32 s7, s6, 6
	s_ashr_i32 s4, s8, 3
	s_cbranch_execz .LBB0_496
	s_branch .LBB0_497
